# GEMM unit head: 128 accumulator zeroing moves -> 64 v_mov_b64 (14 phases)
# speedup vs baseline: 1.0080x; 1.0080x over previous
.LBB0_235:
	s_ashr_i32 s15, s14, 31
	s_lshl_b64 s[16:17], s[14:15], 19
	s_add_u32 s16, s38, s16
	s_addc_u32 s17, s39, s17
	s_and_b64 s[18:19], s[4:5], exec
	s_cselect_b32 s15, s17, s41
	s_cselect_b32 s56, s16, s40
	s_ashr_i32 s13, s12, 31
	s_lshl_b64 s[18:19], s[12:13], 19
	s_add_u32 s18, s3, s18
	s_addc_u32 s19, s30, s19
	s_and_b64 s[28:29], s[4:5], exec
	s_cselect_b32 s13, s19, s23
	s_cselect_b32 s57, s18, s22
	s_add_u32 s58, s22, 0x10000
	s_addc_u32 s59, s23, 0
	s_add_u32 s22, s40, 0x40080
	v_mov_b64_e32 v[2:3], 0
	v_mov_b64_e32 v[4:5], 0
	v_mov_b64_e32 v[6:7], 0
	v_mov_b64_e32 v[8:9], 0
	v_mov_b64_e32 v[10:11], 0
	v_mov_b64_e32 v[12:13], 0
	v_mov_b64_e32 v[14:15], 0
	v_mov_b64_e32 v[16:17], 0
	v_mov_b64_e32 v[18:19], 0
	v_mov_b64_e32 v[20:21], 0
	v_mov_b64_e32 v[22:23], 0
	v_mov_b64_e32 v[24:25], 0
	v_mov_b64_e32 v[26:27], 0
	v_mov_b64_e32 v[28:29], 0
	v_mov_b64_e32 v[30:31], 0
	v_mov_b64_e32 v[32:33], 0
	v_mov_b64_e32 v[34:35], 0
	v_mov_b64_e32 v[36:37], 0
	v_mov_b64_e32 v[38:39], 0
	v_mov_b64_e32 v[40:41], 0
	v_mov_b64_e32 v[42:43], 0
	v_mov_b64_e32 v[44:45], 0
	v_mov_b64_e32 v[46:47], 0
	v_mov_b64_e32 v[48:49], 0
	v_mov_b64_e32 v[50:51], 0
	v_mov_b64_e32 v[52:53], 0
	v_mov_b64_e32 v[54:55], 0
	v_mov_b64_e32 v[56:57], 0
	v_mov_b64_e32 v[58:59], 0
	v_mov_b64_e32 v[60:61], 0
	v_mov_b64_e32 v[62:63], 0
	v_mov_b64_e32 v[64:65], 0
	v_mov_b64_e32 v[66:67], 0
	v_mov_b64_e32 v[68:69], 0
	v_mov_b64_e32 v[70:71], 0
	v_mov_b64_e32 v[72:73], 0
	v_mov_b64_e32 v[74:75], 0
	v_mov_b64_e32 v[76:77], 0
	v_mov_b64_e32 v[78:79], 0
	v_mov_b64_e32 v[80:81], 0
	v_mov_b64_e32 v[82:83], 0
	v_mov_b64_e32 v[84:85], 0
	v_mov_b64_e32 v[86:87], 0
	v_mov_b64_e32 v[88:89], 0
	v_mov_b64_e32 v[90:91], 0
	v_mov_b64_e32 v[92:93], 0
	v_mov_b64_e32 v[94:95], 0
	v_mov_b64_e32 v[96:97], 0
	v_mov_b64_e32 v[98:99], 0
	v_mov_b64_e32 v[100:101], 0
	v_mov_b64_e32 v[102:103], 0
	v_mov_b64_e32 v[104:105], 0
	v_mov_b64_e32 v[106:107], 0
	v_mov_b64_e32 v[108:109], 0
	v_mov_b64_e32 v[110:111], 0
	v_mov_b64_e32 v[112:113], 0
	v_mov_b64_e32 v[114:115], 0
	v_mov_b64_e32 v[116:117], 0
	v_mov_b64_e32 v[118:119], 0
	v_mov_b64_e32 v[120:121], 0
	v_mov_b64_e32 v[122:123], 0
	v_mov_b64_e32 v[124:125], 0
	v_mov_b64_e32 v[126:127], 0
	v_mov_b64_e32 v[128:129], 0
	s_addc_u32 s23, s41, 0
	s_mov_b32 s28, -2

.LBB0_608:
	s_cmp_lt_i32 s42, 0
	s_cselect_b32 s33, 32, 4
	s_add_i32 s43, s33, -2
	s_add_u32 s45, s56, 0x10000
	s_addc_u32 s47, s57, 0
	s_add_u32 s56, s58, 0x80080
	v_mov_b64_e32 v[2:3], 0
	v_mov_b64_e32 v[4:5], 0
	v_mov_b64_e32 v[6:7], 0
	v_mov_b64_e32 v[8:9], 0
	v_mov_b64_e32 v[10:11], 0
	v_mov_b64_e32 v[12:13], 0
	v_mov_b64_e32 v[14:15], 0
	v_mov_b64_e32 v[16:17], 0
	v_mov_b64_e32 v[18:19], 0
	v_mov_b64_e32 v[20:21], 0
	v_mov_b64_e32 v[22:23], 0
	v_mov_b64_e32 v[24:25], 0
	v_mov_b64_e32 v[26:27], 0
	v_mov_b64_e32 v[28:29], 0
	v_mov_b64_e32 v[30:31], 0
	v_mov_b64_e32 v[32:33], 0
	v_mov_b64_e32 v[34:35], 0
	v_mov_b64_e32 v[36:37], 0
	v_mov_b64_e32 v[38:39], 0
	v_mov_b64_e32 v[40:41], 0
	v_mov_b64_e32 v[42:43], 0
	v_mov_b64_e32 v[44:45], 0
	v_mov_b64_e32 v[46:47], 0
	v_mov_b64_e32 v[48:49], 0
	v_mov_b64_e32 v[50:51], 0
	v_mov_b64_e32 v[52:53], 0
	v_mov_b64_e32 v[54:55], 0
	v_mov_b64_e32 v[56:57], 0
	v_mov_b64_e32 v[58:59], 0
	v_mov_b64_e32 v[60:61], 0
	v_mov_b64_e32 v[62:63], 0
	v_mov_b64_e32 v[64:65], 0
	v_mov_b64_e32 v[66:67], 0
	v_mov_b64_e32 v[68:69], 0
	v_mov_b64_e32 v[70:71], 0
	v_mov_b64_e32 v[72:73], 0
	v_mov_b64_e32 v[74:75], 0
	v_mov_b64_e32 v[76:77], 0
	v_mov_b64_e32 v[78:79], 0
	v_mov_b64_e32 v[80:81], 0
	v_mov_b64_e32 v[82:83], 0
	v_mov_b64_e32 v[84:85], 0
	v_mov_b64_e32 v[86:87], 0
	v_mov_b64_e32 v[88:89], 0
	v_mov_b64_e32 v[90:91], 0
	v_mov_b64_e32 v[92:93], 0
	v_mov_b64_e32 v[94:95], 0
	v_mov_b64_e32 v[96:97], 0
	v_mov_b64_e32 v[98:99], 0
	v_mov_b64_e32 v[100:101], 0
	v_mov_b64_e32 v[102:103], 0
	v_mov_b64_e32 v[104:105], 0
	v_mov_b64_e32 v[106:107], 0
	v_mov_b64_e32 v[108:109], 0
	v_mov_b64_e32 v[110:111], 0
	v_mov_b64_e32 v[112:113], 0
	v_mov_b64_e32 v[114:115], 0
	v_mov_b64_e32 v[116:117], 0
	v_mov_b64_e32 v[118:119], 0
	v_mov_b64_e32 v[120:121], 0
	v_mov_b64_e32 v[122:123], 0
	v_mov_b64_e32 v[124:125], 0
	v_mov_b64_e32 v[126:127], 0
	v_mov_b64_e32 v[128:129], 0
	s_mov_b32 s28, 0
	s_addc_u32 s57, s59, 0

.LBB0_738:
	s_ashr_i32 s17, s16, 31
	s_lshl_b64 s[18:19], s[16:17], 19
	s_add_u32 s18, s38, s18
	s_addc_u32 s19, s39, s19
	s_and_b64 s[20:21], s[4:5], exec
	s_cselect_b32 s17, s19, s47
	s_cselect_b32 s43, s18, s46
	s_ashr_i32 s15, s14, 31
	s_lshl_b64 s[20:21], s[14:15], 19
	s_add_u32 s20, s3, s20
	s_addc_u32 s21, s30, s21
	s_and_b64 s[28:29], s[4:5], exec
	s_cselect_b32 s15, s21, s45
	s_cselect_b32 s63, s20, s44
	s_add_u32 s64, s44, 0x10000
	s_addc_u32 s65, s45, 0
	s_add_u32 s44, s46, 0x40080
	v_mov_b64_e32 v[2:3], 0
	v_mov_b64_e32 v[4:5], 0
	v_mov_b64_e32 v[6:7], 0
	v_mov_b64_e32 v[8:9], 0
	v_mov_b64_e32 v[10:11], 0
	v_mov_b64_e32 v[12:13], 0
	v_mov_b64_e32 v[14:15], 0
	v_mov_b64_e32 v[16:17], 0
	v_mov_b64_e32 v[18:19], 0
	v_mov_b64_e32 v[20:21], 0
	v_mov_b64_e32 v[22:23], 0
	v_mov_b64_e32 v[24:25], 0
	v_mov_b64_e32 v[26:27], 0
	v_mov_b64_e32 v[28:29], 0
	v_mov_b64_e32 v[30:31], 0
	v_mov_b64_e32 v[32:33], 0
	v_mov_b64_e32 v[34:35], 0
	v_mov_b64_e32 v[36:37], 0
	v_mov_b64_e32 v[38:39], 0
	v_mov_b64_e32 v[40:41], 0
	v_mov_b64_e32 v[42:43], 0
	v_mov_b64_e32 v[44:45], 0
	v_mov_b64_e32 v[46:47], 0
	v_mov_b64_e32 v[48:49], 0
	v_mov_b64_e32 v[50:51], 0
	v_mov_b64_e32 v[52:53], 0
	v_mov_b64_e32 v[54:55], 0
	v_mov_b64_e32 v[56:57], 0
	v_mov_b64_e32 v[58:59], 0
	v_mov_b64_e32 v[60:61], 0
	v_mov_b64_e32 v[62:63], 0
	v_mov_b64_e32 v[64:65], 0
	v_mov_b64_e32 v[66:67], 0
	v_mov_b64_e32 v[68:69], 0
	v_mov_b64_e32 v[70:71], 0
	v_mov_b64_e32 v[72:73], 0
	v_mov_b64_e32 v[74:75], 0
	v_mov_b64_e32 v[76:77], 0
	v_mov_b64_e32 v[78:79], 0
	v_mov_b64_e32 v[80:81], 0
	v_mov_b64_e32 v[82:83], 0
	v_mov_b64_e32 v[84:85], 0
	v_mov_b64_e32 v[86:87], 0
	v_mov_b64_e32 v[88:89], 0
	v_mov_b64_e32 v[90:91], 0
	v_mov_b64_e32 v[92:93], 0
	v_mov_b64_e32 v[94:95], 0
	v_mov_b64_e32 v[96:97], 0
	v_mov_b64_e32 v[98:99], 0
	v_mov_b64_e32 v[100:101], 0
	v_mov_b64_e32 v[102:103], 0
	v_mov_b64_e32 v[104:105], 0
	v_mov_b64_e32 v[106:107], 0
	v_mov_b64_e32 v[108:109], 0
	v_mov_b64_e32 v[110:111], 0
	v_mov_b64_e32 v[112:113], 0
	v_mov_b64_e32 v[114:115], 0
	v_mov_b64_e32 v[116:117], 0
	v_mov_b64_e32 v[118:119], 0
	v_mov_b64_e32 v[120:121], 0
	v_mov_b64_e32 v[122:123], 0
	v_mov_b64_e32 v[124:125], 0
	v_mov_b64_e32 v[126:127], 0
	v_mov_b64_e32 v[128:129], 0
	s_addc_u32 s45, s47, 0
	s_mov_b32 s28, -2

.LBB0_823:
	s_cmp_lt_i32 s22, 0
	s_cselect_b32 s23, 44, 4
	s_add_i32 s73, s23, -2
	s_add_u32 s46, s46, 0xc000
	s_addc_u32 s47, s47, 0
	s_add_u32 s76, s48, 0x10000
	v_mov_b64_e32 v[2:3], 0
	v_mov_b64_e32 v[4:5], 0
	v_mov_b64_e32 v[6:7], 0
	v_mov_b64_e32 v[8:9], 0
	v_mov_b64_e32 v[10:11], 0
	v_mov_b64_e32 v[12:13], 0
	v_mov_b64_e32 v[14:15], 0
	v_mov_b64_e32 v[16:17], 0
	v_mov_b64_e32 v[18:19], 0
	v_mov_b64_e32 v[20:21], 0
	v_mov_b64_e32 v[22:23], 0
	v_mov_b64_e32 v[24:25], 0
	v_mov_b64_e32 v[26:27], 0
	v_mov_b64_e32 v[28:29], 0
	v_mov_b64_e32 v[30:31], 0
	v_mov_b64_e32 v[32:33], 0
	v_mov_b64_e32 v[34:35], 0
	v_mov_b64_e32 v[36:37], 0
	v_mov_b64_e32 v[38:39], 0
	v_mov_b64_e32 v[40:41], 0
	v_mov_b64_e32 v[42:43], 0
	v_mov_b64_e32 v[44:45], 0
	v_mov_b64_e32 v[46:47], 0
	v_mov_b64_e32 v[48:49], 0
	v_mov_b64_e32 v[50:51], 0
	v_mov_b64_e32 v[52:53], 0
	v_mov_b64_e32 v[54:55], 0
	v_mov_b64_e32 v[56:57], 0
	v_mov_b64_e32 v[58:59], 0
	v_mov_b64_e32 v[60:61], 0
	v_mov_b64_e32 v[62:63], 0
	v_mov_b64_e32 v[64:65], 0
	v_mov_b64_e32 v[66:67], 0
	v_mov_b64_e32 v[68:69], 0
	v_mov_b64_e32 v[70:71], 0
	v_mov_b64_e32 v[72:73], 0
	v_mov_b64_e32 v[74:75], 0
	v_mov_b64_e32 v[76:77], 0
	v_mov_b64_e32 v[78:79], 0
	v_mov_b64_e32 v[80:81], 0
	v_mov_b64_e32 v[82:83], 0
	v_mov_b64_e32 v[84:85], 0
	v_mov_b64_e32 v[86:87], 0
	v_mov_b64_e32 v[88:89], 0
	v_mov_b64_e32 v[90:91], 0
	v_mov_b64_e32 v[92:93], 0
	v_mov_b64_e32 v[94:95], 0
	v_mov_b64_e32 v[96:97], 0
	v_mov_b64_e32 v[98:99], 0
	v_mov_b64_e32 v[100:101], 0
	v_mov_b64_e32 v[102:103], 0
	v_mov_b64_e32 v[104:105], 0
	v_mov_b64_e32 v[106:107], 0
	v_mov_b64_e32 v[108:109], 0
	v_mov_b64_e32 v[110:111], 0
	v_mov_b64_e32 v[112:113], 0
	v_mov_b64_e32 v[114:115], 0
	v_mov_b64_e32 v[116:117], 0
	v_mov_b64_e32 v[118:119], 0
	v_mov_b64_e32 v[120:121], 0
	v_mov_b64_e32 v[122:123], 0
	v_mov_b64_e32 v[124:125], 0
	v_mov_b64_e32 v[126:127], 0
	v_mov_b64_e32 v[128:129], 0
	s_mov_b32 s28, 0
	s_addc_u32 s77, s49, 0

.LBB0_957:
	s_ashr_i32 s19, s18, 31
	s_lshl_b64 s[20:21], s[18:19], 19
	s_add_u32 s20, s38, s20
	s_addc_u32 s21, s39, s21
	s_and_b64 s[22:23], s[4:5], exec
	s_cselect_b32 s19, s21, s45
	s_cselect_b32 s56, s20, s44
	s_ashr_i32 s17, s16, 31
	s_lshl_b64 s[22:23], s[16:17], 19
	s_add_u32 s22, s3, s22
	s_addc_u32 s23, s30, s23
	s_and_b64 s[28:29], s[4:5], exec
	s_cselect_b32 s17, s23, s43
	s_cselect_b32 s57, s22, s42
	s_add_u32 s58, s42, 0x10000
	s_addc_u32 s59, s43, 0
	s_add_u32 s42, s44, 0x40080
	v_mov_b64_e32 v[2:3], 0
	v_mov_b64_e32 v[4:5], 0
	v_mov_b64_e32 v[6:7], 0
	v_mov_b64_e32 v[8:9], 0
	v_mov_b64_e32 v[10:11], 0
	v_mov_b64_e32 v[12:13], 0
	v_mov_b64_e32 v[14:15], 0
	v_mov_b64_e32 v[16:17], 0
	v_mov_b64_e32 v[18:19], 0
	v_mov_b64_e32 v[20:21], 0
	v_mov_b64_e32 v[22:23], 0
	v_mov_b64_e32 v[24:25], 0
	v_mov_b64_e32 v[26:27], 0
	v_mov_b64_e32 v[28:29], 0
	v_mov_b64_e32 v[30:31], 0
	v_mov_b64_e32 v[32:33], 0
	v_mov_b64_e32 v[34:35], 0
	v_mov_b64_e32 v[36:37], 0
	v_mov_b64_e32 v[38:39], 0
	v_mov_b64_e32 v[40:41], 0
	v_mov_b64_e32 v[42:43], 0
	v_mov_b64_e32 v[44:45], 0
	v_mov_b64_e32 v[46:47], 0
	v_mov_b64_e32 v[48:49], 0
	v_mov_b64_e32 v[50:51], 0
	v_mov_b64_e32 v[52:53], 0
	v_mov_b64_e32 v[54:55], 0
	v_mov_b64_e32 v[56:57], 0
	v_mov_b64_e32 v[58:59], 0
	v_mov_b64_e32 v[60:61], 0
	v_mov_b64_e32 v[62:63], 0
	v_mov_b64_e32 v[64:65], 0
	v_mov_b64_e32 v[66:67], 0
	v_mov_b64_e32 v[68:69], 0
	v_mov_b64_e32 v[70:71], 0
	v_mov_b64_e32 v[72:73], 0
	v_mov_b64_e32 v[74:75], 0
	v_mov_b64_e32 v[76:77], 0
	v_mov_b64_e32 v[78:79], 0
	v_mov_b64_e32 v[80:81], 0
	v_mov_b64_e32 v[82:83], 0
	v_mov_b64_e32 v[84:85], 0
	v_mov_b64_e32 v[86:87], 0
	v_mov_b64_e32 v[88:89], 0
	v_mov_b64_e32 v[90:91], 0
	v_mov_b64_e32 v[92:93], 0
	v_mov_b64_e32 v[94:95], 0
	v_mov_b64_e32 v[96:97], 0
	v_mov_b64_e32 v[98:99], 0
	v_mov_b64_e32 v[100:101], 0
	v_mov_b64_e32 v[102:103], 0
	v_mov_b64_e32 v[104:105], 0
	v_mov_b64_e32 v[106:107], 0
	v_mov_b64_e32 v[108:109], 0
	v_mov_b64_e32 v[110:111], 0
	v_mov_b64_e32 v[112:113], 0
	v_mov_b64_e32 v[114:115], 0
	v_mov_b64_e32 v[116:117], 0
	v_mov_b64_e32 v[118:119], 0
	v_mov_b64_e32 v[120:121], 0
	v_mov_b64_e32 v[122:123], 0
	v_mov_b64_e32 v[124:125], 0
	v_mov_b64_e32 v[126:127], 0
	v_mov_b64_e32 v[128:129], 0
	s_addc_u32 s43, s45, 0
	s_mov_b32 s28, -2

.LBB0_1099:
	v_mov_b64_e32 v[2:3], 0
	v_mov_b64_e32 v[4:5], 0
	v_mov_b64_e32 v[6:7], 0
	v_mov_b64_e32 v[8:9], 0
	v_mov_b64_e32 v[10:11], 0
	v_mov_b64_e32 v[12:13], 0
	v_mov_b64_e32 v[14:15], 0
	v_mov_b64_e32 v[16:17], 0
	v_mov_b64_e32 v[18:19], 0
	v_mov_b64_e32 v[20:21], 0
	v_mov_b64_e32 v[22:23], 0
	v_mov_b64_e32 v[24:25], 0
	v_mov_b64_e32 v[26:27], 0
	v_mov_b64_e32 v[28:29], 0
	v_mov_b64_e32 v[30:31], 0
	v_mov_b64_e32 v[32:33], 0
	v_mov_b64_e32 v[34:35], 0
	v_mov_b64_e32 v[36:37], 0
	v_mov_b64_e32 v[38:39], 0
	v_mov_b64_e32 v[40:41], 0
	v_mov_b64_e32 v[42:43], 0
	v_mov_b64_e32 v[44:45], 0
	v_mov_b64_e32 v[46:47], 0
	v_mov_b64_e32 v[48:49], 0
	v_mov_b64_e32 v[50:51], 0
	v_mov_b64_e32 v[52:53], 0
	v_mov_b64_e32 v[54:55], 0
	v_mov_b64_e32 v[56:57], 0
	v_mov_b64_e32 v[58:59], 0
	v_mov_b64_e32 v[60:61], 0
	v_mov_b64_e32 v[62:63], 0
	v_mov_b64_e32 v[64:65], 0
	v_mov_b64_e32 v[66:67], 0
	v_mov_b64_e32 v[68:69], 0
	v_mov_b64_e32 v[70:71], 0
	v_mov_b64_e32 v[72:73], 0
	v_mov_b64_e32 v[74:75], 0
	v_mov_b64_e32 v[76:77], 0
	v_mov_b64_e32 v[78:79], 0
	v_mov_b64_e32 v[80:81], 0
	v_mov_b64_e32 v[82:83], 0
	v_mov_b64_e32 v[84:85], 0
	v_mov_b64_e32 v[86:87], 0
	v_mov_b64_e32 v[88:89], 0
	v_mov_b64_e32 v[90:91], 0
	v_mov_b64_e32 v[92:93], 0
	v_mov_b64_e32 v[94:95], 0
	v_mov_b64_e32 v[96:97], 0
	v_mov_b64_e32 v[98:99], 0
	v_mov_b64_e32 v[100:101], 0
	v_mov_b64_e32 v[102:103], 0
	v_mov_b64_e32 v[104:105], 0
	v_mov_b64_e32 v[106:107], 0
	v_mov_b64_e32 v[108:109], 0
	v_mov_b64_e32 v[110:111], 0
	v_mov_b64_e32 v[112:113], 0
	v_mov_b64_e32 v[114:115], 0
	v_mov_b64_e32 v[116:117], 0
	v_mov_b64_e32 v[118:119], 0
	v_mov_b64_e32 v[120:121], 0
	v_mov_b64_e32 v[122:123], 0
	v_mov_b64_e32 v[124:125], 0
	v_mov_b64_e32 v[126:127], 0
	v_mov_b64_e32 v[128:129], 0
	s_mov_b32 s6, 0
	s_mov_b64 s[50:51], -1
	s_mov_b64 s[52:53], 0

.LBB0_1266:
	s_cmp_lt_i32 s42, 0
	s_cselect_b32 s33, 16, 4
	s_add_i32 s43, s33, -2
	s_add_u32 s45, s56, 0x10000
	s_addc_u32 s47, s57, 0
	s_add_u32 s56, s58, 0x40080
	v_mov_b64_e32 v[2:3], 0
	v_mov_b64_e32 v[4:5], 0
	v_mov_b64_e32 v[6:7], 0
	v_mov_b64_e32 v[8:9], 0
	v_mov_b64_e32 v[10:11], 0
	v_mov_b64_e32 v[12:13], 0
	v_mov_b64_e32 v[14:15], 0
	v_mov_b64_e32 v[16:17], 0
	v_mov_b64_e32 v[18:19], 0
	v_mov_b64_e32 v[20:21], 0
	v_mov_b64_e32 v[22:23], 0
	v_mov_b64_e32 v[24:25], 0
	v_mov_b64_e32 v[26:27], 0
	v_mov_b64_e32 v[28:29], 0
	v_mov_b64_e32 v[30:31], 0
	v_mov_b64_e32 v[32:33], 0
	v_mov_b64_e32 v[34:35], 0
	v_mov_b64_e32 v[36:37], 0
	v_mov_b64_e32 v[38:39], 0
	v_mov_b64_e32 v[40:41], 0
	v_mov_b64_e32 v[42:43], 0
	v_mov_b64_e32 v[44:45], 0
	v_mov_b64_e32 v[46:47], 0
	v_mov_b64_e32 v[48:49], 0
	v_mov_b64_e32 v[50:51], 0
	v_mov_b64_e32 v[52:53], 0
	v_mov_b64_e32 v[54:55], 0
	v_mov_b64_e32 v[56:57], 0
	v_mov_b64_e32 v[58:59], 0
	v_mov_b64_e32 v[60:61], 0
	v_mov_b64_e32 v[62:63], 0
	v_mov_b64_e32 v[64:65], 0
	v_mov_b64_e32 v[66:67], 0
	v_mov_b64_e32 v[68:69], 0
	v_mov_b64_e32 v[70:71], 0
	v_mov_b64_e32 v[72:73], 0
	v_mov_b64_e32 v[74:75], 0
	v_mov_b64_e32 v[76:77], 0
	v_mov_b64_e32 v[78:79], 0
	v_mov_b64_e32 v[80:81], 0
	v_mov_b64_e32 v[82:83], 0
	v_mov_b64_e32 v[84:85], 0
	v_mov_b64_e32 v[86:87], 0
	v_mov_b64_e32 v[88:89], 0
	v_mov_b64_e32 v[90:91], 0
	v_mov_b64_e32 v[92:93], 0
	v_mov_b64_e32 v[94:95], 0
	v_mov_b64_e32 v[96:97], 0
	v_mov_b64_e32 v[98:99], 0
	v_mov_b64_e32 v[100:101], 0
	v_mov_b64_e32 v[102:103], 0
	v_mov_b64_e32 v[104:105], 0
	v_mov_b64_e32 v[106:107], 0
	v_mov_b64_e32 v[108:109], 0
	v_mov_b64_e32 v[110:111], 0
	v_mov_b64_e32 v[112:113], 0
	v_mov_b64_e32 v[114:115], 0
	v_mov_b64_e32 v[116:117], 0
	v_mov_b64_e32 v[118:119], 0
	v_mov_b64_e32 v[120:121], 0
	v_mov_b64_e32 v[122:123], 0
	v_mov_b64_e32 v[124:125], 0
	v_mov_b64_e32 v[126:127], 0
	v_mov_b64_e32 v[128:129], 0
	s_mov_b32 s28, 0
	s_addc_u32 s57, s59, 0

.LBB0_1615:
	s_cmp_lt_i32 s6, 0
	s_cselect_b32 s28, 56, 14
	s_add_i32 s29, s28, -2
	s_add_u32 s62, s62, 0xc000
	v_lshl_add_u64 v[130:131], v[2:3], 0, s[48:49]
	v_mov_b64_e32 v[2:3], 0
	v_mov_b64_e32 v[4:5], 0
	v_mov_b64_e32 v[6:7], 0
	v_mov_b64_e32 v[8:9], 0
	v_mov_b64_e32 v[10:11], 0
	v_mov_b64_e32 v[12:13], 0
	v_mov_b64_e32 v[14:15], 0
	v_mov_b64_e32 v[16:17], 0
	v_mov_b64_e32 v[18:19], 0
	v_mov_b64_e32 v[20:21], 0
	v_mov_b64_e32 v[22:23], 0
	v_mov_b64_e32 v[24:25], 0
	v_mov_b64_e32 v[26:27], 0
	v_mov_b64_e32 v[28:29], 0
	v_mov_b64_e32 v[30:31], 0
	v_mov_b64_e32 v[32:33], 0
	v_mov_b64_e32 v[34:35], 0
	v_mov_b64_e32 v[36:37], 0
	v_mov_b64_e32 v[38:39], 0
	v_mov_b64_e32 v[40:41], 0
	v_mov_b64_e32 v[42:43], 0
	v_mov_b64_e32 v[44:45], 0
	v_mov_b64_e32 v[46:47], 0
	v_mov_b64_e32 v[48:49], 0
	v_mov_b64_e32 v[50:51], 0
	v_mov_b64_e32 v[52:53], 0
	v_mov_b64_e32 v[54:55], 0
	v_mov_b64_e32 v[56:57], 0
	v_mov_b64_e32 v[58:59], 0
	v_mov_b64_e32 v[60:61], 0
	v_mov_b64_e32 v[62:63], 0
	v_mov_b64_e32 v[64:65], 0
	v_mov_b64_e32 v[66:67], 0
	v_mov_b64_e32 v[68:69], 0
	v_mov_b64_e32 v[70:71], 0
	v_mov_b64_e32 v[72:73], 0
	v_mov_b64_e32 v[74:75], 0
	v_mov_b64_e32 v[76:77], 0
	v_mov_b64_e32 v[78:79], 0
	v_mov_b64_e32 v[80:81], 0
	v_mov_b64_e32 v[82:83], 0
	v_mov_b64_e32 v[84:85], 0
	v_mov_b64_e32 v[86:87], 0
	v_mov_b64_e32 v[88:89], 0
	v_mov_b64_e32 v[90:91], 0
	v_mov_b64_e32 v[92:93], 0
	v_mov_b64_e32 v[94:95], 0
	v_mov_b64_e32 v[96:97], 0
	v_mov_b64_e32 v[98:99], 0
	v_mov_b64_e32 v[100:101], 0
	v_mov_b64_e32 v[102:103], 0
	v_mov_b64_e32 v[104:105], 0
	v_mov_b64_e32 v[106:107], 0
	v_mov_b64_e32 v[108:109], 0
	v_mov_b64_e32 v[110:111], 0
	v_mov_b64_e32 v[112:113], 0
	v_mov_b64_e32 v[114:115], 0
	v_mov_b64_e32 v[116:117], 0
	v_mov_b64_e32 v[118:119], 0
	v_mov_b64_e32 v[120:121], 0
	v_mov_b64_e32 v[122:123], 0
	v_mov_b64_e32 v[124:125], 0
	v_mov_b64_e32 v[126:127], 0
	v_mov_b64_e32 v[128:129], 0
	s_mov_b32 s64, 0
	s_addc_u32 s63, s63, 0

.LBB0_1948:
	s_cmp_lt_i32 s40, 0
	s_cselect_b32 s41, 48, 4
	s_add_i32 s73, s41, -2
	s_add_u32 s75, s48, 0x10000
	v_mov_b64_e32 v[2:3], 0
	v_mov_b64_e32 v[4:5], 0
	v_mov_b64_e32 v[6:7], 0
	v_mov_b64_e32 v[8:9], 0
	v_mov_b64_e32 v[10:11], 0
	v_mov_b64_e32 v[12:13], 0
	v_mov_b64_e32 v[14:15], 0
	v_mov_b64_e32 v[16:17], 0
	v_mov_b64_e32 v[18:19], 0
	v_mov_b64_e32 v[20:21], 0
	v_mov_b64_e32 v[22:23], 0
	v_mov_b64_e32 v[24:25], 0
	v_mov_b64_e32 v[26:27], 0
	v_mov_b64_e32 v[28:29], 0
	v_mov_b64_e32 v[30:31], 0
	v_mov_b64_e32 v[32:33], 0
	v_mov_b64_e32 v[34:35], 0
	v_mov_b64_e32 v[36:37], 0
	v_mov_b64_e32 v[38:39], 0
	v_mov_b64_e32 v[40:41], 0
	v_mov_b64_e32 v[42:43], 0
	v_mov_b64_e32 v[44:45], 0
	v_mov_b64_e32 v[46:47], 0
	v_mov_b64_e32 v[48:49], 0
	v_mov_b64_e32 v[50:51], 0
	v_mov_b64_e32 v[52:53], 0
	v_mov_b64_e32 v[54:55], 0
	v_mov_b64_e32 v[56:57], 0
	v_mov_b64_e32 v[58:59], 0
	v_mov_b64_e32 v[60:61], 0
	v_mov_b64_e32 v[62:63], 0
	v_mov_b64_e32 v[64:65], 0
	v_mov_b64_e32 v[66:67], 0
	v_mov_b64_e32 v[68:69], 0
	v_mov_b64_e32 v[70:71], 0
	v_mov_b64_e32 v[72:73], 0
	v_mov_b64_e32 v[74:75], 0
	v_mov_b64_e32 v[76:77], 0
	v_mov_b64_e32 v[78:79], 0
	v_mov_b64_e32 v[80:81], 0
	v_mov_b64_e32 v[82:83], 0
	v_mov_b64_e32 v[84:85], 0
	v_mov_b64_e32 v[86:87], 0
	v_mov_b64_e32 v[88:89], 0
	v_mov_b64_e32 v[90:91], 0
	v_mov_b64_e32 v[92:93], 0
	v_mov_b64_e32 v[94:95], 0
	v_mov_b64_e32 v[96:97], 0
	v_mov_b64_e32 v[98:99], 0
	v_mov_b64_e32 v[100:101], 0
	v_mov_b64_e32 v[102:103], 0
	v_mov_b64_e32 v[104:105], 0
	v_mov_b64_e32 v[106:107], 0
	v_mov_b64_e32 v[108:109], 0
	v_mov_b64_e32 v[110:111], 0
	v_mov_b64_e32 v[112:113], 0
	v_mov_b64_e32 v[114:115], 0
	v_mov_b64_e32 v[116:117], 0
	v_mov_b64_e32 v[118:119], 0
	v_mov_b64_e32 v[120:121], 0
	v_mov_b64_e32 v[122:123], 0
	v_mov_b64_e32 v[124:125], 0
	v_mov_b64_e32 v[126:127], 0
	v_mov_b64_e32 v[128:129], 0
	s_mov_b32 s29, 0
	s_addc_u32 s28, s49, 0

.LBB0_2078:
	s_ashr_i32 s17, s16, 31
	s_lshl_b64 s[18:19], s[16:17], 19
	s_add_u32 s18, s38, s18
	s_addc_u32 s19, s39, s19
	s_and_b64 s[20:21], s[4:5], exec
	s_cselect_b32 s17, s19, s45
	s_cselect_b32 s41, s18, s44
	s_ashr_i32 s15, s14, 31
	s_lshl_b64 s[20:21], s[14:15], 19
	s_add_u32 s20, s3, s20
	s_addc_u32 s21, s30, s21
	s_and_b64 s[28:29], s[4:5], exec
	s_cselect_b32 s15, s21, s43
	s_cselect_b32 s62, s20, s42
	s_add_u32 s63, s42, 0x10000
	s_addc_u32 s64, s43, 0
	s_add_u32 s42, s44, 0x40080
	v_mov_b64_e32 v[2:3], 0
	v_mov_b64_e32 v[4:5], 0
	v_mov_b64_e32 v[6:7], 0
	v_mov_b64_e32 v[8:9], 0
	v_mov_b64_e32 v[10:11], 0
	v_mov_b64_e32 v[12:13], 0
	v_mov_b64_e32 v[14:15], 0
	v_mov_b64_e32 v[16:17], 0
	v_mov_b64_e32 v[18:19], 0
	v_mov_b64_e32 v[20:21], 0
	v_mov_b64_e32 v[22:23], 0
	v_mov_b64_e32 v[24:25], 0
	v_mov_b64_e32 v[26:27], 0
	v_mov_b64_e32 v[28:29], 0
	v_mov_b64_e32 v[30:31], 0
	v_mov_b64_e32 v[32:33], 0
	v_mov_b64_e32 v[34:35], 0
	v_mov_b64_e32 v[36:37], 0
	v_mov_b64_e32 v[38:39], 0
	v_mov_b64_e32 v[40:41], 0
	v_mov_b64_e32 v[42:43], 0
	v_mov_b64_e32 v[44:45], 0
	v_mov_b64_e32 v[46:47], 0
	v_mov_b64_e32 v[48:49], 0
	v_mov_b64_e32 v[50:51], 0
	v_mov_b64_e32 v[52:53], 0
	v_mov_b64_e32 v[54:55], 0
	v_mov_b64_e32 v[56:57], 0
	v_mov_b64_e32 v[58:59], 0
	v_mov_b64_e32 v[60:61], 0
	v_mov_b64_e32 v[62:63], 0
	v_mov_b64_e32 v[64:65], 0
	v_mov_b64_e32 v[66:67], 0
	v_mov_b64_e32 v[68:69], 0
	v_mov_b64_e32 v[70:71], 0
	v_mov_b64_e32 v[72:73], 0
	v_mov_b64_e32 v[74:75], 0
	v_mov_b64_e32 v[76:77], 0
	v_mov_b64_e32 v[78:79], 0
	v_mov_b64_e32 v[80:81], 0
	v_mov_b64_e32 v[82:83], 0
	v_mov_b64_e32 v[84:85], 0
	v_mov_b64_e32 v[86:87], 0
	v_mov_b64_e32 v[88:89], 0
	v_mov_b64_e32 v[90:91], 0
	v_mov_b64_e32 v[92:93], 0
	v_mov_b64_e32 v[94:95], 0
	v_mov_b64_e32 v[96:97], 0
	v_mov_b64_e32 v[98:99], 0
	v_mov_b64_e32 v[100:101], 0
	v_mov_b64_e32 v[102:103], 0
	v_mov_b64_e32 v[104:105], 0
	v_mov_b64_e32 v[106:107], 0
	v_mov_b64_e32 v[108:109], 0
	v_mov_b64_e32 v[110:111], 0
	v_mov_b64_e32 v[112:113], 0
	v_mov_b64_e32 v[114:115], 0
	v_mov_b64_e32 v[116:117], 0
	v_mov_b64_e32 v[118:119], 0
	v_mov_b64_e32 v[120:121], 0
	v_mov_b64_e32 v[122:123], 0
	v_mov_b64_e32 v[124:125], 0
	v_mov_b64_e32 v[126:127], 0
	v_mov_b64_e32 v[128:129], 0
	s_addc_u32 s43, s45, 0
	s_mov_b32 s28, -2

.LBB0_2163:
	s_cmp_lt_i32 s22, 0
	s_cselect_b32 s23, 44, 4
	s_add_i32 s73, s23, -2
	s_add_u32 s44, s44, 0xc000
	s_addc_u32 s45, s45, 0
	s_add_u32 s75, s46, 0x10000
	v_mov_b64_e32 v[2:3], 0
	v_mov_b64_e32 v[4:5], 0
	v_mov_b64_e32 v[6:7], 0
	v_mov_b64_e32 v[8:9], 0
	v_mov_b64_e32 v[10:11], 0
	v_mov_b64_e32 v[12:13], 0
	v_mov_b64_e32 v[14:15], 0
	v_mov_b64_e32 v[16:17], 0
	v_mov_b64_e32 v[18:19], 0
	v_mov_b64_e32 v[20:21], 0
	v_mov_b64_e32 v[22:23], 0
	v_mov_b64_e32 v[24:25], 0
	v_mov_b64_e32 v[26:27], 0
	v_mov_b64_e32 v[28:29], 0
	v_mov_b64_e32 v[30:31], 0
	v_mov_b64_e32 v[32:33], 0
	v_mov_b64_e32 v[34:35], 0
	v_mov_b64_e32 v[36:37], 0
	v_mov_b64_e32 v[38:39], 0
	v_mov_b64_e32 v[40:41], 0
	v_mov_b64_e32 v[42:43], 0
	v_mov_b64_e32 v[44:45], 0
	v_mov_b64_e32 v[46:47], 0
	v_mov_b64_e32 v[48:49], 0
	v_mov_b64_e32 v[50:51], 0
	v_mov_b64_e32 v[52:53], 0
	v_mov_b64_e32 v[54:55], 0
	v_mov_b64_e32 v[56:57], 0
	v_mov_b64_e32 v[58:59], 0
	v_mov_b64_e32 v[60:61], 0
	v_mov_b64_e32 v[62:63], 0
	v_mov_b64_e32 v[64:65], 0
	v_mov_b64_e32 v[66:67], 0
	v_mov_b64_e32 v[68:69], 0
	v_mov_b64_e32 v[70:71], 0
	v_mov_b64_e32 v[72:73], 0
	v_mov_b64_e32 v[74:75], 0
	v_mov_b64_e32 v[76:77], 0
	v_mov_b64_e32 v[78:79], 0
	v_mov_b64_e32 v[80:81], 0
	v_mov_b64_e32 v[82:83], 0
	v_mov_b64_e32 v[84:85], 0
	v_mov_b64_e32 v[86:87], 0
	v_mov_b64_e32 v[88:89], 0
	v_mov_b64_e32 v[90:91], 0
	v_mov_b64_e32 v[92:93], 0
	v_mov_b64_e32 v[94:95], 0
	v_mov_b64_e32 v[96:97], 0
	v_mov_b64_e32 v[98:99], 0
	v_mov_b64_e32 v[100:101], 0
	v_mov_b64_e32 v[102:103], 0
	v_mov_b64_e32 v[104:105], 0
	v_mov_b64_e32 v[106:107], 0
	v_mov_b64_e32 v[108:109], 0
	v_mov_b64_e32 v[110:111], 0
	v_mov_b64_e32 v[112:113], 0
	v_mov_b64_e32 v[114:115], 0
	v_mov_b64_e32 v[116:117], 0
	v_mov_b64_e32 v[118:119], 0
	v_mov_b64_e32 v[120:121], 0
	v_mov_b64_e32 v[122:123], 0
	v_mov_b64_e32 v[124:125], 0
	v_mov_b64_e32 v[126:127], 0
	v_mov_b64_e32 v[128:129], 0
	s_mov_b32 s28, 0
	s_addc_u32 s76, s47, 0

.LBB0_2293:
	s_ashr_i32 s15, s14, 31
	s_lshl_b64 s[16:17], s[14:15], 19
	s_add_u32 s16, s38, s16
	s_addc_u32 s17, s39, s17
	s_and_b64 s[18:19], s[4:5], exec
	s_cselect_b32 s15, s17, s41
	s_cselect_b32 s57, s16, s40
	s_ashr_i32 s13, s12, 31
	s_lshl_b64 s[18:19], s[12:13], 19
	s_add_u32 s18, s3, s18
	s_addc_u32 s19, s30, s19
	s_and_b64 s[28:29], s[4:5], exec
	s_cselect_b32 s13, s19, s23
	s_cselect_b32 s58, s18, s22
	s_add_u32 s59, s22, 0x10000
	s_addc_u32 s60, s23, 0
	s_add_u32 s22, s40, 0x40080
	v_mov_b64_e32 v[2:3], 0
	v_mov_b64_e32 v[4:5], 0
	v_mov_b64_e32 v[6:7], 0
	v_mov_b64_e32 v[8:9], 0
	v_mov_b64_e32 v[10:11], 0
	v_mov_b64_e32 v[12:13], 0
	v_mov_b64_e32 v[14:15], 0
	v_mov_b64_e32 v[16:17], 0
	v_mov_b64_e32 v[18:19], 0
	v_mov_b64_e32 v[20:21], 0
	v_mov_b64_e32 v[22:23], 0
	v_mov_b64_e32 v[24:25], 0
	v_mov_b64_e32 v[26:27], 0
	v_mov_b64_e32 v[28:29], 0
	v_mov_b64_e32 v[30:31], 0
	v_mov_b64_e32 v[32:33], 0
	v_mov_b64_e32 v[34:35], 0
	v_mov_b64_e32 v[36:37], 0
	v_mov_b64_e32 v[38:39], 0
	v_mov_b64_e32 v[40:41], 0
	v_mov_b64_e32 v[42:43], 0
	v_mov_b64_e32 v[44:45], 0
	v_mov_b64_e32 v[46:47], 0
	v_mov_b64_e32 v[48:49], 0
	v_mov_b64_e32 v[50:51], 0
	v_mov_b64_e32 v[52:53], 0
	v_mov_b64_e32 v[54:55], 0
	v_mov_b64_e32 v[56:57], 0
	v_mov_b64_e32 v[58:59], 0
	v_mov_b64_e32 v[60:61], 0
	v_mov_b64_e32 v[62:63], 0
	v_mov_b64_e32 v[64:65], 0
	v_mov_b64_e32 v[66:67], 0
	v_mov_b64_e32 v[68:69], 0
	v_mov_b64_e32 v[70:71], 0
	v_mov_b64_e32 v[72:73], 0
	v_mov_b64_e32 v[74:75], 0
	v_mov_b64_e32 v[76:77], 0
	v_mov_b64_e32 v[78:79], 0
	v_mov_b64_e32 v[80:81], 0
	v_mov_b64_e32 v[82:83], 0
	v_mov_b64_e32 v[84:85], 0
	v_mov_b64_e32 v[86:87], 0
	v_mov_b64_e32 v[88:89], 0
	v_mov_b64_e32 v[90:91], 0
	v_mov_b64_e32 v[92:93], 0
	v_mov_b64_e32 v[94:95], 0
	v_mov_b64_e32 v[96:97], 0
	v_mov_b64_e32 v[98:99], 0
	v_mov_b64_e32 v[100:101], 0
	v_mov_b64_e32 v[102:103], 0
	v_mov_b64_e32 v[104:105], 0
	v_mov_b64_e32 v[106:107], 0
	v_mov_b64_e32 v[108:109], 0
	v_mov_b64_e32 v[110:111], 0
	v_mov_b64_e32 v[112:113], 0
	v_mov_b64_e32 v[114:115], 0
	v_mov_b64_e32 v[116:117], 0
	v_mov_b64_e32 v[118:119], 0
	v_mov_b64_e32 v[120:121], 0
	v_mov_b64_e32 v[122:123], 0
	v_mov_b64_e32 v[124:125], 0
	v_mov_b64_e32 v[126:127], 0
	v_mov_b64_e32 v[128:129], 0
	s_addc_u32 s23, s41, 0
	s_mov_b32 s28, -2

.LBB0_2658:
	s_ashr_i32 s41, s40, 31
	s_lshl_b64 s[28:29], s[40:41], 20
	s_add_u32 s42, s30, s28
	s_addc_u32 s43, s31, s29
	s_and_b64 s[28:29], s[4:5], exec
	s_cselect_b32 s41, s43, s51
	s_cselect_b32 s70, s42, s50
	s_ashr_i32 s23, s22, 31
	s_lshl_b64 s[28:29], s[22:23], 20
	s_add_u32 s44, s36, s28
	s_addc_u32 s45, s37, s29
	s_and_b64 s[28:29], s[4:5], exec
	s_cselect_b32 s23, s45, s49
	s_cselect_b32 s71, s44, s48
	s_add_u32 s72, s48, 0x10000
	s_addc_u32 s73, s49, 0
	s_add_u32 s48, s50, 0x80080
	v_mov_b64_e32 v[2:3], 0
	v_mov_b64_e32 v[4:5], 0
	v_mov_b64_e32 v[6:7], 0
	v_mov_b64_e32 v[8:9], 0
	v_mov_b64_e32 v[10:11], 0
	v_mov_b64_e32 v[12:13], 0
	v_mov_b64_e32 v[14:15], 0
	v_mov_b64_e32 v[16:17], 0
	v_mov_b64_e32 v[18:19], 0
	v_mov_b64_e32 v[20:21], 0
	v_mov_b64_e32 v[22:23], 0
	v_mov_b64_e32 v[24:25], 0
	v_mov_b64_e32 v[26:27], 0
	v_mov_b64_e32 v[28:29], 0
	v_mov_b64_e32 v[30:31], 0
	v_mov_b64_e32 v[32:33], 0
	v_mov_b64_e32 v[34:35], 0
	v_mov_b64_e32 v[36:37], 0
	v_mov_b64_e32 v[38:39], 0
	v_mov_b64_e32 v[40:41], 0
	v_mov_b64_e32 v[42:43], 0
	v_mov_b64_e32 v[44:45], 0
	v_mov_b64_e32 v[46:47], 0
	v_mov_b64_e32 v[48:49], 0
	v_mov_b64_e32 v[50:51], 0
	v_mov_b64_e32 v[52:53], 0
	v_mov_b64_e32 v[54:55], 0
	v_mov_b64_e32 v[56:57], 0
	v_mov_b64_e32 v[58:59], 0
	v_mov_b64_e32 v[60:61], 0
	v_mov_b64_e32 v[62:63], 0
	v_mov_b64_e32 v[64:65], 0
	v_mov_b64_e32 v[66:67], 0
	v_mov_b64_e32 v[68:69], 0
	v_mov_b64_e32 v[70:71], 0
	v_mov_b64_e32 v[72:73], 0
	v_mov_b64_e32 v[74:75], 0
	v_mov_b64_e32 v[76:77], 0
	v_mov_b64_e32 v[78:79], 0
	v_mov_b64_e32 v[80:81], 0
	v_mov_b64_e32 v[82:83], 0
	v_mov_b64_e32 v[84:85], 0
	v_mov_b64_e32 v[86:87], 0
	v_mov_b64_e32 v[88:89], 0
	v_mov_b64_e32 v[90:91], 0
	v_mov_b64_e32 v[92:93], 0
	v_mov_b64_e32 v[94:95], 0
	v_mov_b64_e32 v[96:97], 0
	v_mov_b64_e32 v[98:99], 0
	v_mov_b64_e32 v[100:101], 0
	v_mov_b64_e32 v[102:103], 0
	v_mov_b64_e32 v[104:105], 0
	v_mov_b64_e32 v[106:107], 0
	v_mov_b64_e32 v[108:109], 0
	v_mov_b64_e32 v[110:111], 0
	v_mov_b64_e32 v[112:113], 0
	v_mov_b64_e32 v[114:115], 0
	v_mov_b64_e32 v[116:117], 0
	v_mov_b64_e32 v[118:119], 0
	v_mov_b64_e32 v[120:121], 0
	v_mov_b64_e32 v[138:139], 0
	v_mov_b64_e32 v[140:141], 0
	v_mov_b64_e32 v[142:143], 0
	v_mov_b64_e32 v[144:145], 0
	s_addc_u32 s49, s51, 0
	s_mov_b32 s28, -2

.LBB0_2998:
	s_cmp_lt_i32 s6, 0
	s_cselect_b32 s28, 56, 14
	s_add_i32 s29, s28, -2
	s_add_u32 s58, s58, 0xc000
	v_lshl_add_u64 v[130:131], v[2:3], 0, s[44:45]
	v_mov_b64_e32 v[2:3], 0
	v_mov_b64_e32 v[4:5], 0
	v_mov_b64_e32 v[6:7], 0
	v_mov_b64_e32 v[8:9], 0
	v_mov_b64_e32 v[10:11], 0
	v_mov_b64_e32 v[12:13], 0
	v_mov_b64_e32 v[14:15], 0
	v_mov_b64_e32 v[16:17], 0
	v_mov_b64_e32 v[18:19], 0
	v_mov_b64_e32 v[20:21], 0
	v_mov_b64_e32 v[22:23], 0
	v_mov_b64_e32 v[24:25], 0
	v_mov_b64_e32 v[26:27], 0
	v_mov_b64_e32 v[28:29], 0
	v_mov_b64_e32 v[30:31], 0
	v_mov_b64_e32 v[32:33], 0
	v_mov_b64_e32 v[34:35], 0
	v_mov_b64_e32 v[36:37], 0
	v_mov_b64_e32 v[38:39], 0
	v_mov_b64_e32 v[40:41], 0
	v_mov_b64_e32 v[42:43], 0
	v_mov_b64_e32 v[44:45], 0
	v_mov_b64_e32 v[46:47], 0
	v_mov_b64_e32 v[48:49], 0
	v_mov_b64_e32 v[50:51], 0
	v_mov_b64_e32 v[52:53], 0
	v_mov_b64_e32 v[54:55], 0
	v_mov_b64_e32 v[56:57], 0
	v_mov_b64_e32 v[58:59], 0
	v_mov_b64_e32 v[60:61], 0
	v_mov_b64_e32 v[62:63], 0
	v_mov_b64_e32 v[64:65], 0
	v_mov_b64_e32 v[66:67], 0
	v_mov_b64_e32 v[68:69], 0
	v_mov_b64_e32 v[70:71], 0
	v_mov_b64_e32 v[72:73], 0
	v_mov_b64_e32 v[74:75], 0
	v_mov_b64_e32 v[76:77], 0
	v_mov_b64_e32 v[78:79], 0
	v_mov_b64_e32 v[80:81], 0
	v_mov_b64_e32 v[82:83], 0
	v_mov_b64_e32 v[84:85], 0
	v_mov_b64_e32 v[86:87], 0
	v_mov_b64_e32 v[88:89], 0
	v_mov_b64_e32 v[90:91], 0
	v_mov_b64_e32 v[92:93], 0
	v_mov_b64_e32 v[94:95], 0
	v_mov_b64_e32 v[96:97], 0
	v_mov_b64_e32 v[98:99], 0
	v_mov_b64_e32 v[100:101], 0
	v_mov_b64_e32 v[102:103], 0
	v_mov_b64_e32 v[104:105], 0
	v_mov_b64_e32 v[106:107], 0
	v_mov_b64_e32 v[108:109], 0
	v_mov_b64_e32 v[110:111], 0
	v_mov_b64_e32 v[112:113], 0
	v_mov_b64_e32 v[114:115], 0
	v_mov_b64_e32 v[116:117], 0
	v_mov_b64_e32 v[118:119], 0
	v_mov_b64_e32 v[120:121], 0
	v_mov_b64_e32 v[122:123], 0
	v_mov_b64_e32 v[124:125], 0
	v_mov_b64_e32 v[126:127], 0
	v_mov_b64_e32 v[128:129], 0
	s_mov_b32 s60, 0
	s_addc_u32 s59, s59, 0
